# MLA steady loops: LDS read-slot scalars simplified / prepared in QK MFMA gaps, dead s_nop dropped
# speedup vs baseline: 1.0008x; 1.0008x over previous
; #define SFENCE() __builtin_amdgcn_sched_barrier(0)
; template <bool FOX>
; __device__ __forceinline__ void attn_unit(const Args& A, int b, int h, int qb, LAS char* shm, LAS float* dg) {
;     ...
;           const lds_cptr vp = vp0 + ((t - 1) % NS) * VSLOT; float sa = 0.f, sb = 0.f;
; #pragma unroll
;           for (int g = 0; g < 2 * NQ; ++g) {
;               if (!FOX && g == 0) c0 = __builtin_amdgcn_mfma_f32_32x32x16_bf16(kf[0], qr[0], negm, 0, 0, 0);
;               else if (!FOX && g == 1) c1 = __builtin_amdgcn_mfma_f32_32x32x16_bf16(kf[1], qr[0], negm, 0, 0, 0);
;               else if (g & 1) c1 = __builtin_amdgcn_mfma_f32_32x32x16_bf16(kf[g], qr[g >> 1], c1, 0, 0, 0); else c0 = __builtin_amdgcn_mfma_f32_32x32x16_bf16(kf[g], qr[g >> 1], c0, 0, 0, 0);
;               if (g < 8) { const int i = (g >> 1) + 4 * (g & 1); vlo[i] = vtr(vp + (i >> 2) * 4096 + (i & 3) * 1024); vhi[i] = vtr(vp + (i >> 2) * 4096 + (i & 3) * 1024 + 512);
;                   if (g < 4) { sa += pp0[4 * g]; sb += pp0[4 * g + 1]; sa += pp0[4 * g + 2]; sb += pp0[4 * g + 3]; } else { sa += pp1[4 * g - 16]; sb += pp1[4 * g - 15]; sa += pp1[4 * g - 14]; sb += pp1[4 * g - 13]; }
;                   asm volatile("" : "+v"(sa), "+v"(sb)); }
;               { constexpr int G0 = FOX ? 0 : 4; if (g >= G0) { const int q = 2 * (g - G0);
; #pragma unroll
;                   for (int k = 0; k < 2; ++k) { const int w = q + k; const unsigned pkd = w < 8 ? cvt_pk_bf16(pp0[2 * w], pp0[2 * w + 1]) : cvt_pk_bf16(pp1[2 * w - 16], pp1[2 * w - 15]); pw[w >> 2][w & 3] = pkd; } } }
;               SFENCE();
;           }
;           lrun += sa + sb; }
;         MASKONLY(t);
;         float rm; ROWMAX(rm);
;         bool resc = false;
;         if (__any(rm > THR)) { const float dl = fmaxf(rm, 0.f); mhat += dl;
; #pragma unroll
;             for (int r = 0; r < 16; ++r) { c0[r] -= dl; c1[r] -= dl; }
;             if constexpr (!FOX) {
; #pragma unroll
;                 for (int r = 0; r < 16; ++r) negm[r] = -mhat;
;                 asm volatile("" : "+v"(negm)); }
;             const float f = __builtin_amdgcn_exp2f(-dl); lrun *= f; if (hi == 0) wsf[r32] = f; resc = true; }
;         SFENCE();
;         { const lds_cptr kp = kp0 + ((t + 1) % NS) * KSLOT;
; #pragma unroll
;           for (int g = 0; g < 8; ++g) { const int i = (g >> 1) + 4 * (g & 1);
.Lmla_ss1_in:
	s_mov_b32 m0, s52
	s_nop 0
	global_load_lds_dwordx4 v[234:235], off
	s_add_i32 m0, s52, 0x2000
	s_nop 0
	global_load_lds_dwordx4 v[240:241], off
	s_mov_b32 m0, s53
	s_nop 0
	global_load_lds_dwordx4 v[250:251], off
	s_waitcnt lgkmcnt(0)
	s_and_b32 s27, s42, 0x6000
	v_mfma_f32_32x32x16_bf16 v[114:129], v[206:209], v[138:141], v[82:97]
	v_add_u32_e32 v3, s27, v247
	s_add_u32 s42, s42, 0x2000
	s_addc_u32 s43, s43, 0
	ds_read_b64_tr_b16 v[206:207], v3 offset:49152
	ds_read_b64_tr_b16 v[208:209], v3 offset:49664
	v_add_f32_e32 v4, 0, v67
	v_add_f32_e32 v5, 0, v66
	v_add_f32_e32 v4, v69, v4
	v_add_f32_e32 v5, v68, v5
	v_mfma_f32_32x32x16_bf16 v[98:113], v[194:197], v[138:141], v[82:97]
	ds_read_b64_tr_b16 v[194:195], v3 offset:53248
	ds_read_b64_tr_b16 v[196:197], v3 offset:53760
	v_add_f32_e32 v4, v71, v4
	v_add_f32_e32 v5, v70, v5
	v_add_f32_e32 v4, v73, v4
	v_add_f32_e32 v5, v72, v5
	v_mfma_f32_32x32x16_bf16 v[114:129], v[202:205], v[142:145], v[114:129]
	ds_read_b64_tr_b16 v[202:203], v3 offset:50176
	ds_read_b64_tr_b16 v[204:205], v3 offset:50688
	v_add_f32_e32 v4, v75, v4
	v_add_f32_e32 v5, v74, v5
	v_add_f32_e32 v4, v77, v4
	v_add_f32_e32 v5, v76, v5
	v_mfma_f32_32x32x16_bf16 v[98:113], v[186:189], v[142:145], v[98:113]
	ds_read_b64_tr_b16 v[214:215], v3 offset:54272
	ds_read_b64_tr_b16 v[216:217], v3 offset:54784
	v_add_f32_e32 v4, v79, v4
	v_add_f32_e32 v5, v78, v5
	v_add_f32_e32 v4, v81, v4
	v_add_f32_e32 v5, v80, v5
	v_mfma_f32_32x32x16_bf16 v[114:129], v[198:201], v[146:149], v[114:129]
	s_add_i32 s27, s26, 1
	ds_read_b64_tr_b16 v[210:211], v3 offset:51200
	ds_read_b64_tr_b16 v[212:213], v3 offset:51712
	v_add_f32_e32 v4, v51, v4
	v_add_f32_e32 v5, v50, v5
	v_add_f32_e32 v4, v53, v4
	v_add_f32_e32 v5, v52, v5
	v_mfma_f32_32x32x16_bf16 v[98:113], v[182:185], v[146:149], v[98:113]
	s_and_b32 s47, s27, 3
	ds_read_b64_tr_b16 v[12:13], v3 offset:55296
	ds_read_b64_tr_b16 v[14:15], v3 offset:55808
	v_add_f32_e32 v4, v55, v4
	v_add_f32_e32 v5, v54, v5
	v_add_f32_e32 v4, v57, v4
	v_add_f32_e32 v5, v56, v5
	v_mfma_f32_32x32x16_bf16 v[114:129], v[190:193], v[150:153], v[114:129]
	s_mulk_i32 s47, 0x3000
	ds_read_b64_tr_b16 v[8:9], v3 offset:52224
	ds_read_b64_tr_b16 v[10:11], v3 offset:52736
	v_add_f32_e32 v4, v59, v4
	v_add_f32_e32 v16, v61, v4
	v_add_f32_e32 v4, v58, v5
	v_add_f32_e32 v17, v60, v4
	v_mfma_f32_32x32x16_bf16 v[98:113], v[170:173], v[150:153], v[98:113]
	v_lshl_add_u64 v[234:235], v[234:235], 0, s[62:63]
	s_and_b32 s64, s26, 3
	ds_read_b64_tr_b16 v[4:5], v3 offset:56320
	ds_read_b64_tr_b16 v[6:7], v3 offset:56832
	v_add_f32_e32 v3, v63, v16
	v_add_f32_e32 v16, v62, v17
	v_add_f32_e32 v3, v65, v3
	v_add_f32_e32 v16, v64, v16
	v_mfma_f32_32x32x16_bf16 v[114:129], v[178:181], v[154:157], v[114:129]
	s_mulk_i32 s64, 0x3000
	v_lshl_add_u64 v[250:251], v[232:233], 0, s[42:43]
	v_cvt_pk_bf16_f32 v178, v50, v51
	v_cvt_pk_bf16_f32 v179, v52, v53
	v_cvt_pk_bf16_f32 v186, v66, v67
	v_cvt_pk_bf16_f32 v187, v68, v69
	v_mfma_f32_32x32x16_bf16 v[98:113], v[166:169], v[154:157], v[98:113]
	s_add_i32 s52, s64, s91
	s_add_i32 s64, s42, 0x6000
	v_lshl_add_u64 v[240:241], v[234:235], 0, s[56:57]
	v_cvt_pk_bf16_f32 v180, v54, v55
	v_cvt_pk_bf16_f32 v181, v56, v57
	v_cvt_pk_bf16_f32 v188, v70, v71
	v_cvt_pk_bf16_f32 v189, v72, v73
	v_mfma_f32_32x32x16_bf16 v[114:129], v[174:177], v[158:161], v[114:129]
	s_and_b32 s64, s64, 0x6000
	s_add_i32 s53, s64, s93
	v_cvt_pk_bf16_f32 v218, v58, v59
	v_cvt_pk_bf16_f32 v219, v60, v61
	v_cvt_pk_bf16_f32 v182, v74, v75
	v_cvt_pk_bf16_f32 v183, v76, v77
	v_mfma_f32_32x32x16_bf16 v[98:113], v[162:165], v[158:161], v[98:113]
	v_cvt_pk_bf16_f32 v220, v62, v63
	v_cvt_pk_bf16_f32 v221, v64, v65
	v_cvt_pk_bf16_f32 v184, v78, v79
	v_cvt_pk_bf16_f32 v185, v80, v81
	v_add_f32_e32 v3, v3, v16
	v_add_f32_e32 v246, v246, v3
	s_waitcnt lgkmcnt(0)
	v_mfma_f32_32x32x16_bf16 v[18:33], v[186:189], v[206:209], v[18:33]
	v_exp_f32_e32 v66, v114
	v_exp_f32_e32 v67, v115
	v_exp_f32_e32 v68, v116
	v_exp_f32_e32 v69, v117
	v_add_u32_e32 v3, s47, v248
	v_mfma_f32_32x32x16_bf16 v[34:49], v[186:189], v[194:197], v[34:49]
	v_exp_f32_e32 v70, v118
	v_exp_f32_e32 v71, v119
	v_exp_f32_e32 v72, v120
	v_exp_f32_e32 v73, v121
	ds_read_b128 v[206:209], v3
	ds_read_b128 v[194:197], v3 offset:512
	v_mfma_f32_32x32x16_bf16 v[18:33], v[182:185], v[202:205], v[18:33]
	v_exp_f32_e32 v74, v122
	v_exp_f32_e32 v75, v123
	v_exp_f32_e32 v76, v124
	v_exp_f32_e32 v77, v125
	ds_read_b128 v[202:205], v3 offset:2048
	ds_read_b128 v[186:189], v3 offset:2560
	v_mfma_f32_32x32x16_bf16 v[34:49], v[182:185], v[214:217], v[34:49]
	v_exp_f32_e32 v78, v126
	v_exp_f32_e32 v79, v127
	v_exp_f32_e32 v80, v128
	v_exp_f32_e32 v81, v129
	ds_read_b128 v[198:201], v3 offset:4096
	ds_read_b128 v[182:185], v3 offset:4608
	v_mfma_f32_32x32x16_bf16 v[18:33], v[178:181], v[210:213], v[18:33]
	v_exp_f32_e32 v50, v98
	v_exp_f32_e32 v51, v99
	v_exp_f32_e32 v52, v100
	v_exp_f32_e32 v53, v101
	ds_read_b128 v[190:193], v3 offset:6144
	ds_read_b128 v[170:173], v3 offset:6656
	v_mfma_f32_32x32x16_bf16 v[34:49], v[178:181], v[12:15], v[34:49]
	v_exp_f32_e32 v54, v102
	v_exp_f32_e32 v55, v103
	v_exp_f32_e32 v56, v104
	v_exp_f32_e32 v57, v105
	ds_read_b128 v[178:181], v3 offset:8192
	ds_read_b128 v[166:169], v3 offset:8704
	v_mfma_f32_32x32x16_bf16 v[18:33], v[218:221], v[8:11], v[18:33]
	v_exp_f32_e32 v58, v106
	v_exp_f32_e32 v59, v107
	v_exp_f32_e32 v60, v108
	v_exp_f32_e32 v61, v109
	ds_read_b128 v[174:177], v3 offset:10240
	ds_read_b128 v[162:165], v3 offset:10752
	v_mfma_f32_32x32x16_bf16 v[34:49], v[218:221], v[4:7], v[34:49]
	v_exp_f32_e32 v62, v110
	v_exp_f32_e32 v63, v111
	v_exp_f32_e32 v64, v112
	v_exp_f32_e32 v65, v113
	s_mov_b32 s26, s27
	s_cmp_eq_u32 s27, s96
	s_cbranch_scc1 .Lmla_ss1_xdone
	s_add_i32 s64, s27, 3
	s_cmp_lt_u32 s64, s94
	s_cbranch_scc1 .Lmla_ss1_top
	s_waitcnt vmcnt(4)
	s_barrier
	s_branch .Lmla_ss_back

; #define SFENCE() __builtin_amdgcn_sched_barrier(0)
; template <bool FOX>
; __device__ __forceinline__ void attn_unit(const Args& A, int b, int h, int qb, LAS char* shm, LAS float* dg) {
;     ...
;           const lds_cptr vp = vp0 + ((t - 1) % NS) * VSLOT; float sa = 0.f, sb = 0.f;
; #pragma unroll
;           for (int g = 0; g < 2 * NQ; ++g) {
;               if (!FOX && g == 0) c0 = __builtin_amdgcn_mfma_f32_32x32x16_bf16(kf[0], qr[0], negm, 0, 0, 0);
;               else if (!FOX && g == 1) c1 = __builtin_amdgcn_mfma_f32_32x32x16_bf16(kf[1], qr[0], negm, 0, 0, 0);
;               else if (g & 1) c1 = __builtin_amdgcn_mfma_f32_32x32x16_bf16(kf[g], qr[g >> 1], c1, 0, 0, 0); else c0 = __builtin_amdgcn_mfma_f32_32x32x16_bf16(kf[g], qr[g >> 1], c0, 0, 0, 0);
;               if (g < 8) { const int i = (g >> 1) + 4 * (g & 1); vlo[i] = vtr(vp + (i >> 2) * 4096 + (i & 3) * 1024); vhi[i] = vtr(vp + (i >> 2) * 4096 + (i & 3) * 1024 + 512);
;                   if (g < 4) { sa += pp0[4 * g]; sb += pp0[4 * g + 1]; sa += pp0[4 * g + 2]; sb += pp0[4 * g + 3]; } else { sa += pp1[4 * g - 16]; sb += pp1[4 * g - 15]; sa += pp1[4 * g - 14]; sb += pp1[4 * g - 13]; }
;                   asm volatile("" : "+v"(sa), "+v"(sb)); }
;               { constexpr int G0 = FOX ? 0 : 4; if (g >= G0) { const int q = 2 * (g - G0);
; #pragma unroll
;                   for (int k = 0; k < 2; ++k) { const int w = q + k; const unsigned pkd = w < 8 ? cvt_pk_bf16(pp0[2 * w], pp0[2 * w + 1]) : cvt_pk_bf16(pp1[2 * w - 16], pp1[2 * w - 15]); pw[w >> 2][w & 3] = pkd; } } }
;               SFENCE();
;           }
;           lrun += sa + sb; }
;         MASKONLY(t);
;         float rm; ROWMAX(rm);
;         bool resc = false;
;         if (__any(rm > THR)) { const float dl = fmaxf(rm, 0.f); mhat += dl;
; #pragma unroll
;             for (int r = 0; r < 16; ++r) { c0[r] -= dl; c1[r] -= dl; }
;             if constexpr (!FOX) {
; #pragma unroll
;                 for (int r = 0; r < 16; ++r) negm[r] = -mhat;
;                 asm volatile("" : "+v"(negm)); }
;             const float f = __builtin_amdgcn_exp2f(-dl); lrun *= f; if (hi == 0) wsf[r32] = f; resc = true; }
;         SFENCE();
;         { const lds_cptr kp = kp0 + ((t + 1) % NS) * KSLOT;
; #pragma unroll
;           for (int g = 0; g < 8; ++g) { const int i = (g >> 1) + 4 * (g & 1);
.Lmla_ss2_top:
	s_mov_b32 m0, s52
	s_nop 0
	global_load_lds_dwordx4 v[234:235], off
	s_mov_b32 m0, s53
	s_nop 0
	global_load_lds_dwordx4 v[250:251], off
	s_waitcnt lgkmcnt(0)
	s_and_b32 s27, s42, 0x6000
	v_mfma_f32_32x32x16_bf16 v[114:129], v[206:209], v[138:141], v[82:97]
	v_add_u32_e32 v3, s27, v247
	s_add_u32 s42, s42, 0x2000
	s_addc_u32 s43, s43, 0
	ds_read_b64_tr_b16 v[206:207], v3 offset:49152
	ds_read_b64_tr_b16 v[208:209], v3 offset:49664
	v_add_f32_e32 v4, 0, v67
	v_add_f32_e32 v5, 0, v66
	v_add_f32_e32 v4, v69, v4
	v_add_f32_e32 v5, v68, v5
	v_mfma_f32_32x32x16_bf16 v[98:113], v[194:197], v[138:141], v[82:97]
	ds_read_b64_tr_b16 v[194:195], v3 offset:53248
	ds_read_b64_tr_b16 v[196:197], v3 offset:53760
	v_add_f32_e32 v4, v71, v4
	v_add_f32_e32 v5, v70, v5
	v_add_f32_e32 v4, v73, v4
	v_add_f32_e32 v5, v72, v5
	v_mfma_f32_32x32x16_bf16 v[114:129], v[202:205], v[142:145], v[114:129]
	ds_read_b64_tr_b16 v[202:203], v3 offset:50176
	ds_read_b64_tr_b16 v[204:205], v3 offset:50688
	v_add_f32_e32 v4, v75, v4
	v_add_f32_e32 v5, v74, v5
	v_add_f32_e32 v4, v77, v4
	v_add_f32_e32 v5, v76, v5
	v_mfma_f32_32x32x16_bf16 v[98:113], v[186:189], v[142:145], v[98:113]
	ds_read_b64_tr_b16 v[214:215], v3 offset:54272
	ds_read_b64_tr_b16 v[216:217], v3 offset:54784
	v_add_f32_e32 v4, v79, v4
	v_add_f32_e32 v5, v78, v5
	v_add_f32_e32 v4, v81, v4
	v_add_f32_e32 v5, v80, v5
	v_mfma_f32_32x32x16_bf16 v[114:129], v[198:201], v[146:149], v[114:129]
	s_add_i32 s27, s26, 1
	ds_read_b64_tr_b16 v[210:211], v3 offset:51200
	ds_read_b64_tr_b16 v[212:213], v3 offset:51712
	v_add_f32_e32 v4, v51, v4
	v_add_f32_e32 v5, v50, v5
	v_add_f32_e32 v4, v53, v4
	v_add_f32_e32 v5, v52, v5
	v_mfma_f32_32x32x16_bf16 v[98:113], v[182:185], v[146:149], v[98:113]
	s_and_b32 s47, s27, 3
	ds_read_b64_tr_b16 v[12:13], v3 offset:55296
	ds_read_b64_tr_b16 v[14:15], v3 offset:55808
	v_add_f32_e32 v4, v55, v4
	v_add_f32_e32 v5, v54, v5
	v_add_f32_e32 v4, v57, v4
	v_add_f32_e32 v5, v56, v5
	v_mfma_f32_32x32x16_bf16 v[114:129], v[190:193], v[150:153], v[114:129]
	s_mulk_i32 s47, 0x3000
	ds_read_b64_tr_b16 v[8:9], v3 offset:52224
	ds_read_b64_tr_b16 v[10:11], v3 offset:52736
	v_add_f32_e32 v4, v59, v4
	v_add_f32_e32 v16, v61, v4
	v_add_f32_e32 v4, v58, v5
	v_add_f32_e32 v17, v60, v4
	v_mfma_f32_32x32x16_bf16 v[98:113], v[170:173], v[150:153], v[98:113]
	v_lshl_add_u64 v[234:235], v[234:235], 0, s[62:63]
	s_and_b32 s64, s26, 3
	ds_read_b64_tr_b16 v[4:5], v3 offset:56320
	ds_read_b64_tr_b16 v[6:7], v3 offset:56832
	v_add_f32_e32 v3, v63, v16
	v_add_f32_e32 v16, v62, v17
	v_add_f32_e32 v3, v65, v3
	v_add_f32_e32 v16, v64, v16
	v_mfma_f32_32x32x16_bf16 v[114:129], v[178:181], v[154:157], v[114:129]
	s_mulk_i32 s64, 0x3000
	v_lshl_add_u64 v[250:251], v[232:233], 0, s[42:43]
	v_cvt_pk_bf16_f32 v178, v50, v51
	v_cvt_pk_bf16_f32 v179, v52, v53
	v_cvt_pk_bf16_f32 v186, v66, v67
	v_cvt_pk_bf16_f32 v187, v68, v69
	v_mfma_f32_32x32x16_bf16 v[98:113], v[166:169], v[154:157], v[98:113]
	s_add_i32 s52, s64, s91
	s_add_i32 s64, s42, 0x6000
	v_cvt_pk_bf16_f32 v180, v54, v55
	v_cvt_pk_bf16_f32 v181, v56, v57
	v_cvt_pk_bf16_f32 v188, v70, v71
	v_cvt_pk_bf16_f32 v189, v72, v73
	v_mfma_f32_32x32x16_bf16 v[114:129], v[174:177], v[158:161], v[114:129]
	s_and_b32 s64, s64, 0x6000
	s_add_i32 s53, s64, s93
	v_cvt_pk_bf16_f32 v218, v58, v59
	v_cvt_pk_bf16_f32 v219, v60, v61
	v_cvt_pk_bf16_f32 v182, v74, v75
	v_cvt_pk_bf16_f32 v183, v76, v77
	v_mfma_f32_32x32x16_bf16 v[98:113], v[162:165], v[158:161], v[98:113]
	v_cvt_pk_bf16_f32 v220, v62, v63
	v_cvt_pk_bf16_f32 v221, v64, v65
	v_cvt_pk_bf16_f32 v184, v78, v79
	v_cvt_pk_bf16_f32 v185, v80, v81
	v_add_f32_e32 v3, v3, v16
	v_add_f32_e32 v246, v246, v3
	s_waitcnt vmcnt(3)
	s_waitcnt lgkmcnt(0)
	s_barrier
	v_mfma_f32_32x32x16_bf16 v[18:33], v[186:189], v[206:209], v[18:33]
	v_exp_f32_e32 v66, v114
	v_exp_f32_e32 v67, v115
	v_exp_f32_e32 v68, v116
	v_exp_f32_e32 v69, v117
	v_add_u32_e32 v3, s47, v248
	v_mfma_f32_32x32x16_bf16 v[34:49], v[186:189], v[194:197], v[34:49]
	v_exp_f32_e32 v70, v118
	v_exp_f32_e32 v71, v119
	v_exp_f32_e32 v72, v120
	v_exp_f32_e32 v73, v121
	ds_read_b128 v[206:209], v3
	ds_read_b128 v[194:197], v3 offset:512
	v_mfma_f32_32x32x16_bf16 v[18:33], v[182:185], v[202:205], v[18:33]
	v_exp_f32_e32 v74, v122
	v_exp_f32_e32 v75, v123
	v_exp_f32_e32 v76, v124
	v_exp_f32_e32 v77, v125
	ds_read_b128 v[202:205], v3 offset:2048
	ds_read_b128 v[186:189], v3 offset:2560
	v_mfma_f32_32x32x16_bf16 v[34:49], v[182:185], v[214:217], v[34:49]
	v_exp_f32_e32 v78, v126
	v_exp_f32_e32 v79, v127
	v_exp_f32_e32 v80, v128
	v_exp_f32_e32 v81, v129
	ds_read_b128 v[198:201], v3 offset:4096
	ds_read_b128 v[182:185], v3 offset:4608
	v_mfma_f32_32x32x16_bf16 v[18:33], v[178:181], v[210:213], v[18:33]
	v_exp_f32_e32 v50, v98
	v_exp_f32_e32 v51, v99
	v_exp_f32_e32 v52, v100
	v_exp_f32_e32 v53, v101
	ds_read_b128 v[190:193], v3 offset:6144
	ds_read_b128 v[170:173], v3 offset:6656
	v_mfma_f32_32x32x16_bf16 v[34:49], v[178:181], v[12:15], v[34:49]
	v_exp_f32_e32 v54, v102
	v_exp_f32_e32 v55, v103
	v_exp_f32_e32 v56, v104
	v_exp_f32_e32 v57, v105
	ds_read_b128 v[178:181], v3 offset:8192
	ds_read_b128 v[166:169], v3 offset:8704
	v_mfma_f32_32x32x16_bf16 v[18:33], v[218:221], v[8:11], v[18:33]
	v_exp_f32_e32 v58, v106
	v_exp_f32_e32 v59, v107
	v_exp_f32_e32 v60, v108
	v_exp_f32_e32 v61, v109
	ds_read_b128 v[174:177], v3 offset:10240
	ds_read_b128 v[162:165], v3 offset:10752
	v_mfma_f32_32x32x16_bf16 v[34:49], v[218:221], v[4:7], v[34:49]
	v_exp_f32_e32 v62, v110
	v_exp_f32_e32 v63, v111
	v_exp_f32_e32 v64, v112
	v_exp_f32_e32 v65, v113
	s_mov_b32 s26, s27
	s_cmp_eq_u32 s27, s96
	s_cbranch_scc1 .Lmla_ss2_xdone
	s_add_i32 s64, s27, 3
	s_cmp_lt_u32 s64, s94
	s_cbranch_scc1 .Lmla_ss2_top
	s_branch .Lmla_ss_back
